# grid barriers: the leader invalidates its L1 at arrival (under the wait for the other workgroups) instead of after the release; no cacheable loads run in between
# baseline (speedup 1.0000x reference)
; __device__ __forceinline__ unsigned xb_ld(unsigned* p)              { return __hip_atomic_load(p, __ATOMIC_RELAXED, __HIP_MEMORY_SCOPE_AGENT); }
; __device__ __forceinline__ bool xb_leader(int wave) { return wave == 0 && __builtin_amdgcn_mbcnt_hi(~0u, __builtin_amdgcn_mbcnt_lo(~0u, 0u)) == 0u; }
; __device__ __forceinline__ void xcd_barrier_complete(unsigned* bar, unsigned x, unsigned& nloc, unsigned& nx) {
;     const unsigned G = gridDim.x * gridDim.y * gridDim.z;
;     unsigned sum, cnt, mine, sp = 0u;
;     for (;;) {
;         sum = 0u; cnt = 0u; mine = 0u;
; #pragma unroll
;         for (unsigned j = 0; j < 16; ++j) { const unsigned c = xb_ld(&bar[XB_XCNT(j)]); sum += c; cnt += (c > 0u) ? 1u : 0u; mine = (j == x) ? c : mine; }
; __device__ __forceinline__ void xcd_barrier(const XcdBarrier& b) {
;     asm volatile("s_waitcnt vmcnt(0)" ::: "memory");
;     __syncthreads();
;     if (xb_leader(b.wave)) {
;         unsigned* bar = b.bar;
;         __builtin_amdgcn_s_waitcnt(0);
;         unsigned nloc = b.st[0], nx = b.st[1];
;         if (nloc == 0u) { xcd_barrier_complete(bar, b.x, nloc, nx); b.st[0] = nloc; b.st[1] = nx; }
.LBB0_171:
	s_load_dwordx2 s[4:5], s[94:95], 0xe8
	v_cndmask_b32_e64 v0, 0, 1, s[0:1]
	v_cmp_ne_u32_e64 s[0:1], 1, v0
	s_waitcnt lgkmcnt(0)
	s_cmp_gt_i32 s5, 1
	s_cselect_b64 s[4:5], -1, 0
	s_and_b64 s[2:3], s[2:3], s[4:5]
	v_writelane_b32 v254, s0, 8
	s_andn2_b64 vcc, exec, s[2:3]
	s_nop 0
	v_writelane_b32 v254, s1, 9
	s_cbranch_vccnz .LBB0_238
	s_waitcnt vmcnt(0)
	v_readlane_b32 s0, v254, 8
	v_readlane_b32 s1, v254, 9
	s_and_b64 vcc, exec, s[0:1]
	s_barrier
	s_cbranch_vccnz .LBB0_237
	v_mbcnt_lo_u32_b32 v0, -1, 0
	v_mbcnt_hi_u32_b32 v0, -1, v0
	v_cmp_eq_u32_e32 vcc, 0, v0
	s_and_saveexec_b64 s[0:1], vcc
	s_cbranch_execz .LBB0_236
	s_add_i32 s2, 0, 0x23020
	v_mov_b32_e32 v0, s2
	s_waitcnt vmcnt(0) expcnt(0) lgkmcnt(0)
	buffer_inv sc1
	ds_read_b32 v2, v0
	s_add_i32 s2, 0, 0x23024
	v_mov_b32_e32 v0, s2
	ds_read_b32 v0, v0
	s_waitcnt lgkmcnt(1)
	v_cmp_ne_u32_e32 vcc, 0, v2
	s_cbranch_vccnz .LBB0_189
	v_readlane_b32 s2, v254, 2
	v_readlane_b32 s3, v254, 3
	s_load_dwordx2 s[8:9], s[2:3], 0x4
	v_readlane_b32 s38, v254, 4
	v_readlane_b32 s39, v254, 5
	s_add_u32 s2, s38, 0x4200
	s_addc_u32 s3, s39, 0
	s_add_u32 s6, s38, 0x4400
	s_addc_u32 s7, s39, 0
	s_waitcnt lgkmcnt(0)
	s_mul_i32 s33, s8, s92
	s_add_u32 s8, s38, 0x4500
	s_mul_i32 s33, s33, s9
	s_addc_u32 s9, s39, 0
	s_add_u32 s10, s38, 0x4600
	s_addc_u32 s11, s39, 0
	s_add_u32 s12, s38, 0x4700
	s_addc_u32 s13, s39, 0
	s_add_u32 s14, s38, 0x4800
	s_addc_u32 s15, s39, 0
	s_add_u32 s16, s38, 0x4900
	s_addc_u32 s17, s39, 0
	s_add_u32 s18, s38, 0x4a00
	s_addc_u32 s19, s39, 0
	s_add_u32 s20, s38, 0x4b00
	s_addc_u32 s21, s39, 0
	s_add_u32 s22, s38, 0x4c00
	s_addc_u32 s23, s39, 0
	s_add_u32 s24, s38, 0x4d00
	s_addc_u32 s25, s39, 0
	s_add_u32 s26, s38, 0x4e00
	s_addc_u32 s27, s39, 0
	s_add_u32 s28, s38, 0x4f00
	s_addc_u32 s29, s39, 0
	s_add_u32 s30, s38, 0x5000
	s_addc_u32 s31, s39, 0
	s_add_u32 s34, s38, 0x5100
	s_addc_u32 s35, s39, 0
	s_add_u32 s36, s38, 0x5200
	s_addc_u32 s37, s39, 0
	s_add_u32 s38, s38, 0x5300
	s_addc_u32 s39, s39, 0
	s_mov_b32 s46, 1
	v_mov_b32_e32 v16, 0
	s_branch .LBB0_177

; __device__ __forceinline__ unsigned xb_ld(unsigned* p)              { return __hip_atomic_load(p, __ATOMIC_RELAXED, __HIP_MEMORY_SCOPE_AGENT); }
; #define XB_SPIN(cond, bar) do { unsigned _sp = 0; while (cond) { __builtin_amdgcn_s_sleep(1); \
;     if ((++_sp & 255u) == 0u) { if (xb_ld(&(bar)[XB_TMO])) break; if (_sp > XB_SPIN_CAP) { atomicAdd(&(bar)[XB_TMO], 1u); break; } } } } while (0)
; __device__ __forceinline__ void xcd_barrier(const XcdBarrier& b) {
;     ...
;             XB_SPIN(xb_ld(&bar[XB_XGEN(b.x)]) == gen, bar);
;             __builtin_amdgcn_fence(__ATOMIC_ACQUIRE, "agent");
;             asm volatile("s_waitcnt vmcnt(0)" ::: "memory");
.LBB0_209:
	s_or_b64 exec, exec, s[8:9]
	s_waitcnt vmcnt(0)
	s_waitcnt vmcnt(0)

; __device__ __forceinline__ unsigned xb_add(unsigned* p, unsigned v) { return __hip_atomic_fetch_add(p, v, __ATOMIC_RELAXED, __HIP_MEMORY_SCOPE_AGENT); }
; __device__ __forceinline__ void xcd_barrier(const XcdBarrier& b) {
;     ...
;             __builtin_amdgcn_fence(__ATOMIC_ACQUIRE, "agent");
;             xb_add(&bar[XB_XGEN(b.x)], 1u);
;             asm volatile("s_waitcnt vmcnt(0)" ::: "memory");
.LBB0_233:
	s_or_b64 exec, exec, s[6:7]
	s_mov_b64 s[6:7], exec
	v_mbcnt_lo_u32_b32 v0, s6, 0
	v_mbcnt_hi_u32_b32 v0, s7, v0
	v_cmp_eq_u32_e32 vcc, 0, v0
	s_waitcnt vmcnt(0)
	s_and_saveexec_b64 s[8:9], vcc
	s_cbranch_execz .LBB0_235
	s_bcnt1_i32_b64 s6, s[6:7]
	v_mov_b32_e32 v0, 0x2000
	v_mov_b32_e32 v1, s6
	global_atomic_add v0, v1, s[2:3] offset:1024

; __device__ __forceinline__ unsigned xb_ld(unsigned* p)              { return __hip_atomic_load(p, __ATOMIC_RELAXED, __HIP_MEMORY_SCOPE_AGENT); }
; __device__ __forceinline__ bool xb_leader(int wave) { return wave == 0 && __builtin_amdgcn_mbcnt_hi(~0u, __builtin_amdgcn_mbcnt_lo(~0u, 0u)) == 0u; }
; __device__ __forceinline__ void xcd_barrier_complete(unsigned* bar, unsigned x, unsigned& nloc, unsigned& nx) {
;     const unsigned G = gridDim.x * gridDim.y * gridDim.z;
;     unsigned sum, cnt, mine, sp = 0u;
;     for (;;) {
;         sum = 0u; cnt = 0u; mine = 0u;
; #pragma unroll
;         for (unsigned j = 0; j < 16; ++j) { const unsigned c = xb_ld(&bar[XB_XCNT(j)]); sum += c; cnt += (c > 0u) ? 1u : 0u; mine = (j == x) ? c : mine; }
; __device__ __forceinline__ void xcd_barrier(const XcdBarrier& b) {
;     asm volatile("s_waitcnt vmcnt(0)" ::: "memory");
;     __syncthreads();
;     if (xb_leader(b.wave)) {
;         unsigned* bar = b.bar;
;         __builtin_amdgcn_s_waitcnt(0);
;         unsigned nloc = b.st[0], nx = b.st[1];
;         if (nloc == 0u) { xcd_barrier_complete(bar, b.x, nloc, nx); b.st[0] = nloc; b.st[1] = nx; }
.LBB0_382:
	s_load_dwordx2 s[2:3], s[94:95], 0xe8
	s_waitcnt lgkmcnt(0)
	s_cmp_gt_i32 s3, 2
	s_cselect_b64 s[2:3], -1, 0
	s_and_b64 s[0:1], s[0:1], s[2:3]
	s_andn2_b64 vcc, exec, s[0:1]
	s_cbranch_vccnz .LBB0_438
	s_waitcnt vmcnt(0)
	v_readlane_b32 s0, v254, 8
	v_readlane_b32 s1, v254, 9
	s_and_b64 vcc, exec, s[0:1]
	s_waitcnt vmcnt(0)
	s_barrier
	s_cbranch_vccnz .LBB0_437
	v_mbcnt_lo_u32_b32 v0, -1, 0
	v_mbcnt_hi_u32_b32 v0, -1, v0
	v_cmp_eq_u32_e32 vcc, 0, v0
	s_and_saveexec_b64 s[0:1], vcc
	s_cbranch_execz .LBB0_436
	s_add_i32 s2, 0, 0x23020
	v_mov_b32_e32 v0, s2
	s_waitcnt vmcnt(0) expcnt(0) lgkmcnt(0)
	buffer_inv sc1
	ds_read_b32 v2, v0
	s_add_i32 s2, 0, 0x23024
	v_mov_b32_e32 v0, s2
	ds_read_b32 v0, v0
	s_waitcnt lgkmcnt(1)
	v_cmp_ne_u32_e32 vcc, 0, v2
	s_cbranch_vccnz .LBB0_400
	v_readlane_b32 s2, v254, 2
	v_readlane_b32 s3, v254, 3
	s_load_dwordx2 s[6:7], s[2:3], 0x4
	v_readlane_b32 s36, v254, 4
	v_readlane_b32 s37, v254, 5
	s_add_u32 s2, s36, 0x4200
	s_addc_u32 s3, s37, 0
	s_add_u32 s4, s36, 0x4400
	s_addc_u32 s5, s37, 0
	s_waitcnt lgkmcnt(0)
	s_mul_i32 s33, s6, s92
	s_add_u32 s6, s36, 0x4500
	s_mul_i32 s33, s33, s7
	s_addc_u32 s7, s37, 0
	s_add_u32 s8, s36, 0x4600
	s_addc_u32 s9, s37, 0
	s_add_u32 s10, s36, 0x4700
	s_addc_u32 s11, s37, 0
	s_add_u32 s12, s36, 0x4800
	s_addc_u32 s13, s37, 0
	s_add_u32 s14, s36, 0x4900
	s_addc_u32 s15, s37, 0
	s_add_u32 s16, s36, 0x4a00
	s_addc_u32 s17, s37, 0
	s_add_u32 s18, s36, 0x4b00
	s_addc_u32 s19, s37, 0
	s_add_u32 s20, s36, 0x4c00
	s_addc_u32 s21, s37, 0
	s_add_u32 s22, s36, 0x4d00
	s_addc_u32 s23, s37, 0
	s_add_u32 s24, s36, 0x4e00
	s_addc_u32 s25, s37, 0
	s_add_u32 s26, s36, 0x4f00
	s_addc_u32 s27, s37, 0
	s_add_u32 s28, s36, 0x5000
	s_addc_u32 s29, s37, 0
	s_add_u32 s30, s36, 0x5100
	s_addc_u32 s31, s37, 0
	s_add_u32 s34, s36, 0x5200
	s_addc_u32 s35, s37, 0
	s_add_u32 s36, s36, 0x5300
	s_addc_u32 s37, s37, 0
	s_mov_b32 s44, 1
	v_mov_b32_e32 v16, 0
	s_branch .LBB0_388

; __device__ __forceinline__ unsigned xb_ld(unsigned* p)              { return __hip_atomic_load(p, __ATOMIC_RELAXED, __HIP_MEMORY_SCOPE_AGENT); }
; #define XB_SPIN(cond, bar) do { unsigned _sp = 0; while (cond) { __builtin_amdgcn_s_sleep(1); \
;     if ((++_sp & 255u) == 0u) { if (xb_ld(&(bar)[XB_TMO])) break; if (_sp > XB_SPIN_CAP) { atomicAdd(&(bar)[XB_TMO], 1u); break; } } } } while (0)
; __device__ __forceinline__ void xcd_barrier(const XcdBarrier& b) {
;     ...
;             XB_SPIN(xb_ld(&bar[XB_XGEN(b.x)]) == gen, bar);
;             __builtin_amdgcn_fence(__ATOMIC_ACQUIRE, "agent");
;             asm volatile("s_waitcnt vmcnt(0)" ::: "memory");
.LBB0_415:
	s_or_b64 exec, exec, s[6:7]
	s_waitcnt vmcnt(0)
	s_waitcnt vmcnt(0)

; __device__ __forceinline__ unsigned xb_add(unsigned* p, unsigned v) { return __hip_atomic_fetch_add(p, v, __ATOMIC_RELAXED, __HIP_MEMORY_SCOPE_AGENT); }
; __device__ __forceinline__ void xcd_barrier(const XcdBarrier& b) {
;     ...
;             __builtin_amdgcn_fence(__ATOMIC_ACQUIRE, "agent");
;             xb_add(&bar[XB_XGEN(b.x)], 1u);
;             asm volatile("s_waitcnt vmcnt(0)" ::: "memory");
.LBB0_433:
	s_or_b64 exec, exec, s[4:5]
	s_mov_b64 s[4:5], exec
	v_mbcnt_lo_u32_b32 v0, s4, 0
	v_mbcnt_hi_u32_b32 v0, s5, v0
	v_cmp_eq_u32_e32 vcc, 0, v0
	s_waitcnt vmcnt(0)
	s_and_saveexec_b64 s[6:7], vcc
	s_cbranch_execz .LBB0_435
	s_bcnt1_i32_b64 s4, s[4:5]
	v_mov_b32_e32 v0, 0x2000
	v_mov_b32_e32 v1, s4
	global_atomic_add v0, v1, s[2:3] offset:1024

; __device__ __forceinline__ unsigned xb_ld(unsigned* p)              { return __hip_atomic_load(p, __ATOMIC_RELAXED, __HIP_MEMORY_SCOPE_AGENT); }
; __device__ __forceinline__ bool xb_leader(int wave) { return wave == 0 && __builtin_amdgcn_mbcnt_hi(~0u, __builtin_amdgcn_mbcnt_lo(~0u, 0u)) == 0u; }
; __device__ __forceinline__ void xcd_barrier_complete(unsigned* bar, unsigned x, unsigned& nloc, unsigned& nx) {
;     const unsigned G = gridDim.x * gridDim.y * gridDim.z;
;     unsigned sum, cnt, mine, sp = 0u;
;     for (;;) {
;         sum = 0u; cnt = 0u; mine = 0u;
; #pragma unroll
;         for (unsigned j = 0; j < 16; ++j) { const unsigned c = xb_ld(&bar[XB_XCNT(j)]); sum += c; cnt += (c > 0u) ? 1u : 0u; mine = (j == x) ? c : mine; }
; __device__ __forceinline__ void xcd_barrier(const XcdBarrier& b) {
;     asm volatile("s_waitcnt vmcnt(0)" ::: "memory");
;     __syncthreads();
;     if (xb_leader(b.wave)) {
;         unsigned* bar = b.bar;
;         __builtin_amdgcn_s_waitcnt(0);
;         unsigned nloc = b.st[0], nx = b.st[1];
;         if (nloc == 0u) { xcd_barrier_complete(bar, b.x, nloc, nx); b.st[0] = nloc; b.st[1] = nx; }
.LBB0_1083:
	v_readlane_b32 s0, v254, 0
	v_readlane_b32 s1, v254, 1
	s_cmp_gt_i32 s1, 4
	v_readlane_b32 s0, v254, 35
	s_cselect_b64 s[2:3], -1, 0
	v_readlane_b32 s1, v254, 36
	s_and_b64 s[0:1], s[0:1], s[2:3]
	s_andn2_b64 vcc, exec, s[0:1]
	s_cbranch_vccnz .LBB0_1139
	s_waitcnt vmcnt(0)
	v_readlane_b32 s0, v254, 8
	v_readlane_b32 s1, v254, 9
	s_and_b64 vcc, exec, s[0:1]
	s_waitcnt vmcnt(0) lgkmcnt(0)
	s_barrier
	s_cbranch_vccnz .LBB0_1138
	v_mbcnt_lo_u32_b32 v0, -1, 0
	v_mbcnt_hi_u32_b32 v0, -1, v0
	v_cmp_eq_u32_e32 vcc, 0, v0
	s_and_saveexec_b64 s[0:1], vcc
	s_cbranch_execz .LBB0_1137
	s_add_i32 s4, 0, 0x23020
	v_mov_b32_e32 v0, s4
	s_waitcnt vmcnt(0) expcnt(0) lgkmcnt(0)
	buffer_inv sc1
	ds_read_b32 v2, v0
	s_add_i32 s4, 0, 0x23024
	v_mov_b32_e32 v0, s4
	ds_read_b32 v0, v0
	s_waitcnt lgkmcnt(1)
	v_cmp_ne_u32_e32 vcc, 0, v2
	s_cbranch_vccnz .LBB0_1101
	v_readlane_b32 s4, v254, 2
	v_readlane_b32 s5, v254, 3
	s_load_dwordx2 s[8:9], s[4:5], 0x4
	v_readlane_b32 s38, v254, 4
	v_readlane_b32 s39, v254, 5
	s_add_u32 s4, s38, 0x4200
	s_addc_u32 s5, s39, 0
	s_add_u32 s6, s38, 0x4400
	s_addc_u32 s7, s39, 0
	s_waitcnt lgkmcnt(0)
	s_mul_i32 s33, s8, s92
	s_add_u32 s8, s38, 0x4500
	s_mul_i32 s33, s33, s9
	s_addc_u32 s9, s39, 0
	s_add_u32 s10, s38, 0x4600
	s_addc_u32 s11, s39, 0
	s_add_u32 s12, s38, 0x4700
	s_addc_u32 s13, s39, 0
	s_add_u32 s14, s38, 0x4800
	s_addc_u32 s15, s39, 0
	s_add_u32 s16, s38, 0x4900
	s_addc_u32 s17, s39, 0
	s_add_u32 s18, s38, 0x4a00
	s_addc_u32 s19, s39, 0
	s_add_u32 s20, s38, 0x4b00
	s_addc_u32 s21, s39, 0
	s_add_u32 s22, s38, 0x4c00
	s_addc_u32 s23, s39, 0
	s_add_u32 s24, s38, 0x4d00
	s_addc_u32 s25, s39, 0
	s_add_u32 s26, s38, 0x4e00
	s_addc_u32 s27, s39, 0
	s_add_u32 s28, s38, 0x4f00
	s_addc_u32 s29, s39, 0
	s_add_u32 s30, s38, 0x5000
	s_addc_u32 s31, s39, 0
	s_add_u32 s34, s38, 0x5100
	s_addc_u32 s35, s39, 0
	s_add_u32 s36, s38, 0x5200
	s_addc_u32 s37, s39, 0
	s_add_u32 s38, s38, 0x5300
	s_addc_u32 s39, s39, 0
	s_mov_b32 s46, 1
	v_mov_b32_e32 v16, 0
	s_branch .LBB0_1089

; __device__ __forceinline__ unsigned xb_add(unsigned* p, unsigned v) { return __hip_atomic_fetch_add(p, v, __ATOMIC_RELAXED, __HIP_MEMORY_SCOPE_AGENT); }
; __device__ __forceinline__ void xcd_barrier(const XcdBarrier& b) {
;     ...
;             __builtin_amdgcn_fence(__ATOMIC_ACQUIRE, "agent");
;             xb_add(&bar[XB_XGEN(b.x)], 1u);
;             asm volatile("s_waitcnt vmcnt(0)" ::: "memory");
.LBB0_1134:
	s_or_b64 exec, exec, s[6:7]
	s_mov_b64 s[6:7], exec
	v_mbcnt_lo_u32_b32 v0, s6, 0
	v_mbcnt_hi_u32_b32 v0, s7, v0
	v_cmp_eq_u32_e32 vcc, 0, v0
	s_waitcnt vmcnt(0)
	s_and_saveexec_b64 s[8:9], vcc
	s_cbranch_execz .LBB0_1136
	s_bcnt1_i32_b64 s6, s[6:7]
	v_mov_b32_e32 v0, 0x2000
	v_mov_b32_e32 v1, s6
	global_atomic_add v0, v1, s[4:5] offset:1024

; __device__ __forceinline__ unsigned xb_ld(unsigned* p)              { return __hip_atomic_load(p, __ATOMIC_RELAXED, __HIP_MEMORY_SCOPE_AGENT); }
; __device__ __forceinline__ bool xb_leader(int wave) { return wave == 0 && __builtin_amdgcn_mbcnt_hi(~0u, __builtin_amdgcn_mbcnt_lo(~0u, 0u)) == 0u; }
; __device__ __forceinline__ void xcd_barrier_complete(unsigned* bar, unsigned x, unsigned& nloc, unsigned& nx) {
;     const unsigned G = gridDim.x * gridDim.y * gridDim.z;
;     unsigned sum, cnt, mine, sp = 0u;
;     for (;;) {
;         sum = 0u; cnt = 0u; mine = 0u;
; #pragma unroll
;         for (unsigned j = 0; j < 16; ++j) { const unsigned c = xb_ld(&bar[XB_XCNT(j)]); sum += c; cnt += (c > 0u) ? 1u : 0u; mine = (j == x) ? c : mine; }
; __device__ __forceinline__ void xcd_barrier(const XcdBarrier& b) {
;     asm volatile("s_waitcnt vmcnt(0)" ::: "memory");
;     __syncthreads();
;     if (xb_leader(b.wave)) {
;         unsigned* bar = b.bar;
;         __builtin_amdgcn_s_waitcnt(0);
;         unsigned nloc = b.st[0], nx = b.st[1];
;         if (nloc == 0u) { xcd_barrier_complete(bar, b.x, nloc, nx); b.st[0] = nloc; b.st[1] = nx; }
.LBB0_1181:
	v_readlane_b32 s2, v254, 0
	v_readlane_b32 s3, v254, 1
	s_cmp_gt_i32 s3, 5
	s_cselect_b64 s[2:3], -1, 0
	s_and_b64 s[0:1], s[0:1], s[2:3]
	s_andn2_b64 vcc, exec, s[0:1]
	s_cbranch_vccnz .LBB0_1237
	s_waitcnt vmcnt(0)
	v_readlane_b32 s0, v254, 8
	v_readlane_b32 s1, v254, 9
	s_and_b64 vcc, exec, s[0:1]
	s_waitcnt vmcnt(0) lgkmcnt(0)
	s_barrier
	s_cbranch_vccnz .LBB0_1236
	v_mbcnt_lo_u32_b32 v0, -1, 0
	v_mbcnt_hi_u32_b32 v0, -1, v0
	v_cmp_eq_u32_e32 vcc, 0, v0
	s_and_saveexec_b64 s[0:1], vcc
	s_cbranch_execz .LBB0_1235
	s_add_i32 s6, 0, 0x23020
	v_mov_b32_e32 v0, s6
	s_waitcnt vmcnt(0) expcnt(0) lgkmcnt(0)
	buffer_inv sc1
	ds_read_b32 v2, v0
	s_add_i32 s6, 0, 0x23024
	v_mov_b32_e32 v0, s6
	ds_read_b32 v0, v0
	s_waitcnt lgkmcnt(1)
	v_cmp_ne_u32_e32 vcc, 0, v2
	s_cbranch_vccnz .LBB0_1199
	v_readlane_b32 s6, v254, 2
	v_readlane_b32 s7, v254, 3
	s_load_dwordx2 s[10:11], s[6:7], 0x4
	v_readlane_b32 s40, v254, 4
	v_readlane_b32 s41, v254, 5
	s_add_u32 s6, s40, 0x4200
	s_addc_u32 s7, s41, 0
	s_add_u32 s8, s40, 0x4400
	s_addc_u32 s9, s41, 0
	s_waitcnt lgkmcnt(0)
	s_mul_i32 s48, s10, s92
	s_add_u32 s10, s40, 0x4500
	s_mul_i32 s48, s48, s11
	s_addc_u32 s11, s41, 0
	s_add_u32 s12, s40, 0x4600
	s_addc_u32 s13, s41, 0
	s_add_u32 s14, s40, 0x4700
	s_addc_u32 s15, s41, 0
	s_add_u32 s16, s40, 0x4800
	s_addc_u32 s17, s41, 0
	s_add_u32 s18, s40, 0x4900
	s_addc_u32 s19, s41, 0
	s_add_u32 s20, s40, 0x4a00
	s_addc_u32 s21, s41, 0
	s_add_u32 s22, s40, 0x4b00
	s_addc_u32 s23, s41, 0
	s_add_u32 s24, s40, 0x4c00
	s_addc_u32 s25, s41, 0
	s_add_u32 s26, s40, 0x4d00
	s_addc_u32 s27, s41, 0
	s_add_u32 s28, s40, 0x4e00
	s_addc_u32 s29, s41, 0
	s_add_u32 s30, s40, 0x4f00
	s_addc_u32 s31, s41, 0
	s_add_u32 s34, s40, 0x5000
	s_addc_u32 s35, s41, 0
	s_add_u32 s36, s40, 0x5100
	s_addc_u32 s37, s41, 0
	s_add_u32 s38, s40, 0x5200
	s_addc_u32 s39, s41, 0
	s_add_u32 s40, s40, 0x5300
	s_addc_u32 s41, s41, 0
	s_mov_b32 s49, 1
	v_mov_b32_e32 v16, 0
	s_branch .LBB0_1187

; __device__ __forceinline__ unsigned xb_ld(unsigned* p)              { return __hip_atomic_load(p, __ATOMIC_RELAXED, __HIP_MEMORY_SCOPE_AGENT); }
; #define XB_SPIN(cond, bar) do { unsigned _sp = 0; while (cond) { __builtin_amdgcn_s_sleep(1); \
;     if ((++_sp & 255u) == 0u) { if (xb_ld(&(bar)[XB_TMO])) break; if (_sp > XB_SPIN_CAP) { atomicAdd(&(bar)[XB_TMO], 1u); break; } } } } while (0)
; __device__ __forceinline__ void xcd_barrier(const XcdBarrier& b) {
;     ...
;             XB_SPIN(xb_ld(&bar[XB_XGEN(b.x)]) == gen, bar);
;             __builtin_amdgcn_fence(__ATOMIC_ACQUIRE, "agent");
;             asm volatile("s_waitcnt vmcnt(0)" ::: "memory");
.LBB0_1214:
	s_or_b64 exec, exec, s[10:11]
	s_waitcnt vmcnt(0)
	s_waitcnt vmcnt(0)

; __device__ __forceinline__ unsigned xb_add(unsigned* p, unsigned v) { return __hip_atomic_fetch_add(p, v, __ATOMIC_RELAXED, __HIP_MEMORY_SCOPE_AGENT); }
; __device__ __forceinline__ void xcd_barrier(const XcdBarrier& b) {
;     ...
;             __builtin_amdgcn_fence(__ATOMIC_ACQUIRE, "agent");
;             xb_add(&bar[XB_XGEN(b.x)], 1u);
;             asm volatile("s_waitcnt vmcnt(0)" ::: "memory");
.LBB0_1232:
	s_or_b64 exec, exec, s[8:9]
	s_mov_b64 s[8:9], exec
	v_mbcnt_lo_u32_b32 v0, s8, 0
	v_mbcnt_hi_u32_b32 v0, s9, v0
	v_cmp_eq_u32_e32 vcc, 0, v0
	s_waitcnt vmcnt(0)
	s_and_saveexec_b64 s[10:11], vcc
	s_cbranch_execz .LBB0_1234
	s_bcnt1_i32_b64 s8, s[8:9]
	v_mov_b32_e32 v0, 0x2000
	v_mov_b32_e32 v1, s8
	global_atomic_add v0, v1, s[6:7] offset:1024

; __device__ __forceinline__ unsigned xb_ld(unsigned* p)              { return __hip_atomic_load(p, __ATOMIC_RELAXED, __HIP_MEMORY_SCOPE_AGENT); }
; __device__ __forceinline__ bool xb_leader(int wave) { return wave == 0 && __builtin_amdgcn_mbcnt_hi(~0u, __builtin_amdgcn_mbcnt_lo(~0u, 0u)) == 0u; }
; __device__ __forceinline__ void xcd_barrier_complete(unsigned* bar, unsigned x, unsigned& nloc, unsigned& nx) {
;     const unsigned G = gridDim.x * gridDim.y * gridDim.z;
;     unsigned sum, cnt, mine, sp = 0u;
;     for (;;) {
;         sum = 0u; cnt = 0u; mine = 0u;
; #pragma unroll
;         for (unsigned j = 0; j < 16; ++j) { const unsigned c = xb_ld(&bar[XB_XCNT(j)]); sum += c; cnt += (c > 0u) ? 1u : 0u; mine = (j == x) ? c : mine; }
; __device__ __forceinline__ void xcd_barrier(const XcdBarrier& b) {
;     asm volatile("s_waitcnt vmcnt(0)" ::: "memory");
;     __syncthreads();
;     if (xb_leader(b.wave)) {
;         unsigned* bar = b.bar;
;         __builtin_amdgcn_s_waitcnt(0);
;         unsigned nloc = b.st[0], nx = b.st[1];
;         if (nloc == 0u) { xcd_barrier_complete(bar, b.x, nloc, nx); b.st[0] = nloc; b.st[1] = nx; }
.LBB0_1259:
	v_readlane_b32 s2, v254, 0
	v_readlane_b32 s3, v254, 1
	s_cmp_gt_i32 s3, 6
	s_cselect_b64 s[2:3], -1, 0
	s_and_b64 s[0:1], s[0:1], s[2:3]
	s_andn2_b64 vcc, exec, s[0:1]
	s_cbranch_vccnz .LBB0_1315
	s_waitcnt vmcnt(0)
	v_readlane_b32 s0, v254, 8
	v_readlane_b32 s1, v254, 9
	s_and_b64 vcc, exec, s[0:1]
	s_waitcnt vmcnt(0) lgkmcnt(0)
	s_barrier
	s_cbranch_vccnz .LBB0_1314
	v_mbcnt_lo_u32_b32 v0, -1, 0
	v_mbcnt_hi_u32_b32 v0, -1, v0
	v_cmp_eq_u32_e32 vcc, 0, v0
	s_and_saveexec_b64 s[0:1], vcc
	s_cbranch_execz .LBB0_1313
	s_add_i32 s6, 0, 0x23020
	v_mov_b32_e32 v0, s6
	s_waitcnt vmcnt(0) expcnt(0) lgkmcnt(0)
	buffer_inv sc1
	ds_read_b32 v2, v0
	s_add_i32 s6, 0, 0x23024
	v_mov_b32_e32 v0, s6
	ds_read_b32 v0, v0
	s_waitcnt lgkmcnt(1)
	v_cmp_ne_u32_e32 vcc, 0, v2
	s_cbranch_vccnz .LBB0_1277
	v_readlane_b32 s6, v254, 2
	v_readlane_b32 s7, v254, 3
	s_load_dwordx2 s[10:11], s[6:7], 0x4
	v_readlane_b32 s42, v254, 4
	v_readlane_b32 s43, v254, 5
	s_add_u32 s6, s42, 0x4200
	s_addc_u32 s7, s43, 0
	s_add_u32 s8, s42, 0x4400
	s_addc_u32 s9, s43, 0
	s_waitcnt lgkmcnt(0)
	s_mul_i32 s50, s10, s92
	s_add_u32 s10, s42, 0x4500
	s_mul_i32 s50, s50, s11
	s_addc_u32 s11, s43, 0
	s_add_u32 s12, s42, 0x4600
	s_addc_u32 s13, s43, 0
	s_add_u32 s14, s42, 0x4700
	s_addc_u32 s15, s43, 0
	s_add_u32 s16, s42, 0x4800
	s_addc_u32 s17, s43, 0
	s_add_u32 s18, s42, 0x4900
	s_addc_u32 s19, s43, 0
	s_add_u32 s20, s42, 0x4a00
	s_addc_u32 s21, s43, 0
	s_add_u32 s22, s42, 0x4b00
	s_addc_u32 s23, s43, 0
	s_add_u32 s24, s42, 0x4c00
	s_addc_u32 s25, s43, 0
	s_add_u32 s26, s42, 0x4d00
	s_addc_u32 s27, s43, 0
	s_add_u32 s28, s42, 0x4e00
	s_addc_u32 s29, s43, 0
	s_add_u32 s30, s42, 0x4f00
	s_addc_u32 s31, s43, 0
	s_add_u32 s34, s42, 0x5000
	s_addc_u32 s35, s43, 0
	s_add_u32 s36, s42, 0x5100
	s_addc_u32 s37, s43, 0
	s_add_u32 s40, s42, 0x5200
	s_addc_u32 s41, s43, 0
	s_add_u32 s42, s42, 0x5300
	s_addc_u32 s43, s43, 0
	s_mov_b32 s51, 1
	v_mov_b32_e32 v16, 0
	s_branch .LBB0_1265

; __device__ __forceinline__ unsigned xb_add(unsigned* p, unsigned v) { return __hip_atomic_fetch_add(p, v, __ATOMIC_RELAXED, __HIP_MEMORY_SCOPE_AGENT); }
; __device__ __forceinline__ void xcd_barrier(const XcdBarrier& b) {
;     ...
;             __builtin_amdgcn_fence(__ATOMIC_ACQUIRE, "agent");
;             xb_add(&bar[XB_XGEN(b.x)], 1u);
;             asm volatile("s_waitcnt vmcnt(0)" ::: "memory");
.Lxcdlocal_0:
	s_mov_b64 s[8:9], exec
	v_mbcnt_lo_u32_b32 v0, s8, 0
	v_mbcnt_hi_u32_b32 v0, s9, v0
	v_cmp_eq_u32_e32 vcc, 0, v0
	s_waitcnt vmcnt(0)
	s_and_saveexec_b64 s[10:11], vcc
	s_cbranch_execz .LBB0_1312
	s_bcnt1_i32_b64 s8, s[8:9]
	v_mov_b32_e32 v0, 0x2000
	v_mov_b32_e32 v1, s8
	global_atomic_add v0, v1, s[6:7] offset:1024

; __device__ __forceinline__ unsigned xb_ld(unsigned* p)              { return __hip_atomic_load(p, __ATOMIC_RELAXED, __HIP_MEMORY_SCOPE_AGENT); }
; __device__ __forceinline__ bool xb_leader(int wave) { return wave == 0 && __builtin_amdgcn_mbcnt_hi(~0u, __builtin_amdgcn_mbcnt_lo(~0u, 0u)) == 0u; }
; __device__ __forceinline__ void xcd_barrier_complete(unsigned* bar, unsigned x, unsigned& nloc, unsigned& nx) {
;     const unsigned G = gridDim.x * gridDim.y * gridDim.z;
;     unsigned sum, cnt, mine, sp = 0u;
;     for (;;) {
;         sum = 0u; cnt = 0u; mine = 0u;
; #pragma unroll
;         for (unsigned j = 0; j < 16; ++j) { const unsigned c = xb_ld(&bar[XB_XCNT(j)]); sum += c; cnt += (c > 0u) ? 1u : 0u; mine = (j == x) ? c : mine; }
; __device__ __forceinline__ void xcd_barrier(const XcdBarrier& b) {
;     asm volatile("s_waitcnt vmcnt(0)" ::: "memory");
;     __syncthreads();
;     if (xb_leader(b.wave)) {
;         unsigned* bar = b.bar;
;         __builtin_amdgcn_s_waitcnt(0);
;         unsigned nloc = b.st[0], nx = b.st[1];
;         if (nloc == 0u) { xcd_barrier_complete(bar, b.x, nloc, nx); b.st[0] = nloc; b.st[1] = nx; }
.LBB0_1361:
	v_readlane_b32 s2, v254, 0
	v_readlane_b32 s3, v254, 1
	s_cmp_gt_i32 s3, 7
	s_cselect_b64 s[2:3], -1, 0
	s_and_b64 s[0:1], s[0:1], s[2:3]
	s_andn2_b64 vcc, exec, s[0:1]
	s_cbranch_vccnz .LBB0_1417
	s_waitcnt vmcnt(0)
	v_readlane_b32 s0, v254, 8
	v_readlane_b32 s1, v254, 9
	s_and_b64 vcc, exec, s[0:1]
	s_waitcnt vmcnt(0) lgkmcnt(0)
	s_barrier
	s_cbranch_vccnz .LBB0_1416
	v_mbcnt_lo_u32_b32 v0, -1, 0
	v_mbcnt_hi_u32_b32 v0, -1, v0
	v_cmp_eq_u32_e32 vcc, 0, v0
	s_and_saveexec_b64 s[0:1], vcc
	s_cbranch_execz .LBB0_1415
	s_add_i32 s6, 0, 0x23020
	v_mov_b32_e32 v0, s6
	s_waitcnt vmcnt(0) expcnt(0) lgkmcnt(0)
	buffer_inv sc1
	ds_read_b32 v2, v0
	s_add_i32 s6, 0, 0x23024
	v_mov_b32_e32 v0, s6
	ds_read_b32 v0, v0
	s_waitcnt lgkmcnt(1)
	v_cmp_ne_u32_e32 vcc, 0, v2
	s_cbranch_vccnz .LBB0_1379
	v_readlane_b32 s6, v254, 2
	v_readlane_b32 s7, v254, 3
	s_load_dwordx2 s[10:11], s[6:7], 0x4
	v_readlane_b32 s42, v254, 4
	v_readlane_b32 s43, v254, 5
	s_add_u32 s6, s42, 0x4200
	s_addc_u32 s7, s43, 0
	s_add_u32 s8, s42, 0x4400
	s_addc_u32 s9, s43, 0
	s_waitcnt lgkmcnt(0)
	s_mul_i32 s33, s10, s92
	s_add_u32 s10, s42, 0x4500
	s_mul_i32 s33, s33, s11
	s_addc_u32 s11, s43, 0
	s_add_u32 s12, s42, 0x4600
	s_addc_u32 s13, s43, 0
	s_add_u32 s14, s42, 0x4700
	s_addc_u32 s15, s43, 0
	s_add_u32 s16, s42, 0x4800
	s_addc_u32 s17, s43, 0
	s_add_u32 s18, s42, 0x4900
	s_addc_u32 s19, s43, 0
	s_add_u32 s20, s42, 0x4a00
	s_addc_u32 s21, s43, 0
	s_add_u32 s22, s42, 0x4b00
	s_addc_u32 s23, s43, 0
	s_add_u32 s24, s42, 0x4c00
	s_addc_u32 s25, s43, 0
	s_add_u32 s26, s42, 0x4d00
	s_addc_u32 s27, s43, 0
	s_add_u32 s28, s42, 0x4e00
	s_addc_u32 s29, s43, 0
	s_add_u32 s30, s42, 0x4f00
	s_addc_u32 s31, s43, 0
	s_add_u32 s34, s42, 0x5000
	s_addc_u32 s35, s43, 0
	s_add_u32 s36, s42, 0x5100
	s_addc_u32 s37, s43, 0
	s_add_u32 s40, s42, 0x5200
	s_addc_u32 s41, s43, 0
	s_add_u32 s42, s42, 0x5300
	s_addc_u32 s43, s43, 0
	s_mov_b32 s50, 1
	v_mov_b32_e32 v16, 0
	s_branch .LBB0_1367

; __device__ __forceinline__ unsigned xb_ld(unsigned* p)              { return __hip_atomic_load(p, __ATOMIC_RELAXED, __HIP_MEMORY_SCOPE_AGENT); }
; __device__ __forceinline__ bool xb_leader(int wave) { return wave == 0 && __builtin_amdgcn_mbcnt_hi(~0u, __builtin_amdgcn_mbcnt_lo(~0u, 0u)) == 0u; }
; __device__ __forceinline__ void xcd_barrier_complete(unsigned* bar, unsigned x, unsigned& nloc, unsigned& nx) {
;     const unsigned G = gridDim.x * gridDim.y * gridDim.z;
;     unsigned sum, cnt, mine, sp = 0u;
;     for (;;) {
;         sum = 0u; cnt = 0u; mine = 0u;
; #pragma unroll
;         for (unsigned j = 0; j < 16; ++j) { const unsigned c = xb_ld(&bar[XB_XCNT(j)]); sum += c; cnt += (c > 0u) ? 1u : 0u; mine = (j == x) ? c : mine; }
; __device__ __forceinline__ void xcd_barrier(const XcdBarrier& b) {
;     asm volatile("s_waitcnt vmcnt(0)" ::: "memory");
;     __syncthreads();
;     if (xb_leader(b.wave)) {
;         unsigned* bar = b.bar;
;         __builtin_amdgcn_s_waitcnt(0);
;         unsigned nloc = b.st[0], nx = b.st[1];
;         if (nloc == 0u) { xcd_barrier_complete(bar, b.x, nloc, nx); b.st[0] = nloc; b.st[1] = nx; }
.LBB0_1521:
	v_readlane_b32 s2, v254, 0
	v_readlane_b32 s3, v254, 1
	s_cmp_gt_i32 s3, 8
	s_cselect_b64 s[2:3], -1, 0
	s_and_b64 s[0:1], s[0:1], s[2:3]
	s_andn2_b64 vcc, exec, s[0:1]
	s_cbranch_vccnz .LBB0_1577
	s_waitcnt vmcnt(0)
	v_readlane_b32 s0, v254, 8
	v_readlane_b32 s1, v254, 9
	s_and_b64 vcc, exec, s[0:1]
	s_waitcnt vmcnt(0) lgkmcnt(0)
	s_barrier
	s_cbranch_vccnz .LBB0_1576
	v_mbcnt_lo_u32_b32 v0, -1, 0
	v_mbcnt_hi_u32_b32 v0, -1, v0
	v_cmp_eq_u32_e32 vcc, 0, v0
	s_and_saveexec_b64 s[0:1], vcc
	s_cbranch_execz .LBB0_1575
	s_add_i32 s2, 0, 0x23020
	v_mov_b32_e32 v0, s2
	s_waitcnt vmcnt(0) expcnt(0) lgkmcnt(0)
	buffer_inv sc1
	ds_read_b32 v2, v0
	s_add_i32 s2, 0, 0x23024
	v_mov_b32_e32 v0, s2
	ds_read_b32 v0, v0
	s_waitcnt lgkmcnt(1)
	v_cmp_ne_u32_e32 vcc, 0, v2
	s_cbranch_vccnz .LBB0_1539
	v_readlane_b32 s2, v254, 2
	v_readlane_b32 s3, v254, 3
	s_load_dwordx2 s[10:11], s[2:3], 0x4
	v_readlane_b32 s42, v254, 4
	v_readlane_b32 s43, v254, 5
	s_add_u32 s2, s42, 0x4200
	s_addc_u32 s3, s43, 0
	s_add_u32 s8, s42, 0x4400
	s_addc_u32 s9, s43, 0
	s_waitcnt lgkmcnt(0)
	s_mul_i32 s50, s10, s92
	s_add_u32 s10, s42, 0x4500
	s_mul_i32 s50, s50, s11
	s_addc_u32 s11, s43, 0
	s_add_u32 s12, s42, 0x4600
	s_addc_u32 s13, s43, 0
	s_add_u32 s14, s42, 0x4700
	s_addc_u32 s15, s43, 0
	s_add_u32 s16, s42, 0x4800
	s_addc_u32 s17, s43, 0
	s_add_u32 s18, s42, 0x4900
	s_addc_u32 s19, s43, 0
	s_add_u32 s20, s42, 0x4a00
	s_addc_u32 s21, s43, 0
	s_add_u32 s22, s42, 0x4b00
	s_addc_u32 s23, s43, 0
	s_add_u32 s24, s42, 0x4c00
	s_addc_u32 s25, s43, 0
	s_add_u32 s26, s42, 0x4d00
	s_addc_u32 s27, s43, 0
	s_add_u32 s28, s42, 0x4e00
	s_addc_u32 s29, s43, 0
	s_add_u32 s30, s42, 0x4f00
	s_addc_u32 s31, s43, 0
	s_add_u32 s34, s42, 0x5000
	s_addc_u32 s35, s43, 0
	s_add_u32 s36, s42, 0x5100
	s_addc_u32 s37, s43, 0
	s_add_u32 s40, s42, 0x5200
	s_addc_u32 s41, s43, 0
	s_add_u32 s42, s42, 0x5300
	s_addc_u32 s43, s43, 0
	s_mov_b32 s51, 1
	v_mov_b32_e32 v16, 0
	s_branch .LBB0_1527

; __device__ __forceinline__ unsigned xb_add(unsigned* p, unsigned v) { return __hip_atomic_fetch_add(p, v, __ATOMIC_RELAXED, __HIP_MEMORY_SCOPE_AGENT); }
; __device__ __forceinline__ void xcd_barrier(const XcdBarrier& b) {
;     ...
;             __builtin_amdgcn_fence(__ATOMIC_ACQUIRE, "agent");
;             xb_add(&bar[XB_XGEN(b.x)], 1u);
;             asm volatile("s_waitcnt vmcnt(0)" ::: "memory");
.Lxcdlocal_1:
	s_mov_b64 s[8:9], exec
	v_mbcnt_lo_u32_b32 v0, s8, 0
	v_mbcnt_hi_u32_b32 v0, s9, v0
	v_cmp_eq_u32_e32 vcc, 0, v0
	s_waitcnt vmcnt(0)
	s_and_saveexec_b64 s[10:11], vcc
	s_cbranch_execz .LBB0_1574
	s_bcnt1_i32_b64 s8, s[8:9]
	v_mov_b32_e32 v0, 0x2000
	v_mov_b32_e32 v1, s8
	global_atomic_add v0, v1, s[2:3] offset:1024

; __device__ __forceinline__ unsigned xb_ld(unsigned* p)              { return __hip_atomic_load(p, __ATOMIC_RELAXED, __HIP_MEMORY_SCOPE_AGENT); }
; __device__ __forceinline__ bool xb_leader(int wave) { return wave == 0 && __builtin_amdgcn_mbcnt_hi(~0u, __builtin_amdgcn_mbcnt_lo(~0u, 0u)) == 0u; }
; __device__ __forceinline__ void xcd_barrier_complete(unsigned* bar, unsigned x, unsigned& nloc, unsigned& nx) {
;     const unsigned G = gridDim.x * gridDim.y * gridDim.z;
;     unsigned sum, cnt, mine, sp = 0u;
;     for (;;) {
;         sum = 0u; cnt = 0u; mine = 0u;
; #pragma unroll
;         for (unsigned j = 0; j < 16; ++j) { const unsigned c = xb_ld(&bar[XB_XCNT(j)]); sum += c; cnt += (c > 0u) ? 1u : 0u; mine = (j == x) ? c : mine; }
; __device__ __forceinline__ void xcd_barrier(const XcdBarrier& b) {
;     asm volatile("s_waitcnt vmcnt(0)" ::: "memory");
;     __syncthreads();
;     if (xb_leader(b.wave)) {
;         unsigned* bar = b.bar;
;         __builtin_amdgcn_s_waitcnt(0);
;         unsigned nloc = b.st[0], nx = b.st[1];
;         if (nloc == 0u) { xcd_barrier_complete(bar, b.x, nloc, nx); b.st[0] = nloc; b.st[1] = nx; }
.LBB0_1678:
	v_readlane_b32 s2, v254, 0
	v_readlane_b32 s3, v254, 1
	s_cmp_gt_i32 s3, 10
	s_cselect_b64 s[2:3], -1, 0
	s_and_b64 s[0:1], s[0:1], s[2:3]
	s_andn2_b64 vcc, exec, s[0:1]
	s_cbranch_vccnz .LBB0_1734
	s_waitcnt vmcnt(0)
	v_readlane_b32 s0, v254, 8
	v_readlane_b32 s1, v254, 9
	s_and_b64 vcc, exec, s[0:1]
	s_waitcnt vmcnt(0) lgkmcnt(0)
	s_barrier
	s_cbranch_vccnz .LBB0_1733
	v_mbcnt_lo_u32_b32 v0, -1, 0
	v_mbcnt_hi_u32_b32 v0, -1, v0
	v_cmp_eq_u32_e32 vcc, 0, v0
	s_and_saveexec_b64 s[0:1], vcc
	s_cbranch_execz .LBB0_1732
	s_add_i32 s2, 0, 0x23020
	v_mov_b32_e32 v0, s2
	s_waitcnt vmcnt(0) expcnt(0) lgkmcnt(0)
	buffer_inv sc1
	ds_read_b32 v2, v0
	s_add_i32 s2, 0, 0x23024
	v_mov_b32_e32 v0, s2
	ds_read_b32 v0, v0
	s_waitcnt lgkmcnt(1)
	v_cmp_ne_u32_e32 vcc, 0, v2
	s_cbranch_vccnz .LBB0_1696
	v_readlane_b32 s2, v254, 2
	v_readlane_b32 s3, v254, 3
	s_load_dwordx2 s[8:9], s[2:3], 0x4
	v_readlane_b32 s40, v254, 4
	v_readlane_b32 s41, v254, 5
	s_add_u32 s2, s40, 0x4200
	s_addc_u32 s3, s41, 0
	s_add_u32 s6, s40, 0x4400
	s_addc_u32 s7, s41, 0
	s_waitcnt lgkmcnt(0)
	s_mul_i32 s33, s8, s92
	s_add_u32 s8, s40, 0x4500
	s_mul_i32 s33, s33, s9
	s_addc_u32 s9, s41, 0
	s_add_u32 s10, s40, 0x4600
	s_addc_u32 s11, s41, 0
	s_add_u32 s12, s40, 0x4700
	s_addc_u32 s13, s41, 0
	s_add_u32 s14, s40, 0x4800
	s_addc_u32 s15, s41, 0
	s_add_u32 s16, s40, 0x4900
	s_addc_u32 s17, s41, 0
	s_add_u32 s18, s40, 0x4a00
	s_addc_u32 s19, s41, 0
	s_add_u32 s20, s40, 0x4b00
	s_addc_u32 s21, s41, 0
	s_add_u32 s22, s40, 0x4c00
	s_addc_u32 s23, s41, 0
	s_add_u32 s24, s40, 0x4d00
	s_addc_u32 s25, s41, 0
	s_add_u32 s26, s40, 0x4e00
	s_addc_u32 s27, s41, 0
	s_add_u32 s28, s40, 0x4f00
	s_addc_u32 s29, s41, 0
	s_add_u32 s30, s40, 0x5000
	s_addc_u32 s31, s41, 0
	s_add_u32 s34, s40, 0x5100
	s_addc_u32 s35, s41, 0
	s_add_u32 s36, s40, 0x5200
	s_addc_u32 s37, s41, 0
	s_add_u32 s40, s40, 0x5300
	s_addc_u32 s41, s41, 0
	s_mov_b32 s48, 1
	v_mov_b32_e32 v16, 0
	s_branch .LBB0_1684

; __device__ __forceinline__ unsigned xb_add(unsigned* p, unsigned v) { return __hip_atomic_fetch_add(p, v, __ATOMIC_RELAXED, __HIP_MEMORY_SCOPE_AGENT); }
; __device__ __forceinline__ void xcd_barrier(const XcdBarrier& b) {
;     ...
;             __builtin_amdgcn_fence(__ATOMIC_ACQUIRE, "agent");
;             xb_add(&bar[XB_XGEN(b.x)], 1u);
;             asm volatile("s_waitcnt vmcnt(0)" ::: "memory");
.Lxcdlocal_2:
	s_mov_b64 s[6:7], exec
	v_mbcnt_lo_u32_b32 v0, s6, 0
	v_mbcnt_hi_u32_b32 v0, s7, v0
	v_cmp_eq_u32_e32 vcc, 0, v0
	s_waitcnt vmcnt(0)
	s_and_saveexec_b64 s[8:9], vcc
	s_cbranch_execz .LBB0_1731
	s_bcnt1_i32_b64 s6, s[6:7]
	v_mov_b32_e32 v0, 0x2000
	v_mov_b32_e32 v1, s6
	global_atomic_add v0, v1, s[2:3] offset:1024

; __device__ __forceinline__ unsigned xb_ld(unsigned* p)              { return __hip_atomic_load(p, __ATOMIC_RELAXED, __HIP_MEMORY_SCOPE_AGENT); }
; __device__ __forceinline__ bool xb_leader(int wave) { return wave == 0 && __builtin_amdgcn_mbcnt_hi(~0u, __builtin_amdgcn_mbcnt_lo(~0u, 0u)) == 0u; }
; __device__ __forceinline__ void xcd_barrier_complete(unsigned* bar, unsigned x, unsigned& nloc, unsigned& nx) {
;     const unsigned G = gridDim.x * gridDim.y * gridDim.z;
;     unsigned sum, cnt, mine, sp = 0u;
;     for (;;) {
;         sum = 0u; cnt = 0u; mine = 0u;
; #pragma unroll
;         for (unsigned j = 0; j < 16; ++j) { const unsigned c = xb_ld(&bar[XB_XCNT(j)]); sum += c; cnt += (c > 0u) ? 1u : 0u; mine = (j == x) ? c : mine; }
; __device__ __forceinline__ void xcd_barrier(const XcdBarrier& b) {
;     asm volatile("s_waitcnt vmcnt(0)" ::: "memory");
;     __syncthreads();
;     if (xb_leader(b.wave)) {
;         unsigned* bar = b.bar;
;         __builtin_amdgcn_s_waitcnt(0);
;         unsigned nloc = b.st[0], nx = b.st[1];
;         if (nloc == 0u) { xcd_barrier_complete(bar, b.x, nloc, nx); b.st[0] = nloc; b.st[1] = nx; }
.LBB0_1756:
	v_readlane_b32 s2, v254, 0
	v_readlane_b32 s3, v254, 1
	s_cmp_gt_i32 s3, 14
	s_cselect_b64 s[2:3], -1, 0
	s_and_b64 s[0:1], s[0:1], s[2:3]
	s_andn2_b64 vcc, exec, s[0:1]
	s_cbranch_vccnz .LBB0_1812
	s_waitcnt vmcnt(0)
	v_readlane_b32 s0, v254, 8
	v_readlane_b32 s1, v254, 9
	s_and_b64 vcc, exec, s[0:1]
	s_waitcnt vmcnt(0) lgkmcnt(0)
	s_barrier
	s_cbranch_vccnz .LBB0_1811
	v_mbcnt_lo_u32_b32 v0, -1, 0
	v_mbcnt_hi_u32_b32 v0, -1, v0
	v_cmp_eq_u32_e32 vcc, 0, v0
	s_and_saveexec_b64 s[0:1], vcc
	s_cbranch_execz .LBB0_1810
	s_add_i32 s4, 0, 0x23020
	v_mov_b32_e32 v0, s4
	s_waitcnt vmcnt(0) expcnt(0) lgkmcnt(0)
	buffer_inv sc1
	ds_read_b32 v2, v0
	s_add_i32 s4, 0, 0x23024
	v_mov_b32_e32 v0, s4
	ds_read_b32 v0, v0
	s_waitcnt lgkmcnt(1)
	v_cmp_ne_u32_e32 vcc, 0, v2
	s_cbranch_vccnz .LBB0_1774
	v_readlane_b32 s4, v254, 2
	v_readlane_b32 s5, v254, 3
	s_load_dwordx2 s[8:9], s[4:5], 0x4
	v_readlane_b32 s40, v254, 4
	v_readlane_b32 s41, v254, 5
	s_add_u32 s4, s40, 0x4200
	s_addc_u32 s5, s41, 0
	s_add_u32 s6, s40, 0x4400
	s_addc_u32 s7, s41, 0
	s_waitcnt lgkmcnt(0)
	s_mul_i32 s33, s8, s92
	s_add_u32 s8, s40, 0x4500
	s_mul_i32 s33, s33, s9
	s_addc_u32 s9, s41, 0
	s_add_u32 s10, s40, 0x4600
	s_addc_u32 s11, s41, 0
	s_add_u32 s12, s40, 0x4700
	s_addc_u32 s13, s41, 0
	s_add_u32 s14, s40, 0x4800
	s_addc_u32 s15, s41, 0
	s_add_u32 s16, s40, 0x4900
	s_addc_u32 s17, s41, 0
	s_add_u32 s18, s40, 0x4a00
	s_addc_u32 s19, s41, 0
	s_add_u32 s20, s40, 0x4b00
	s_addc_u32 s21, s41, 0
	s_add_u32 s22, s40, 0x4c00
	s_addc_u32 s23, s41, 0
	s_add_u32 s24, s40, 0x4d00
	s_addc_u32 s25, s41, 0
	s_add_u32 s26, s40, 0x4e00
	s_addc_u32 s27, s41, 0
	s_add_u32 s28, s40, 0x4f00
	s_addc_u32 s29, s41, 0
	s_add_u32 s30, s40, 0x5000
	s_addc_u32 s31, s41, 0
	s_add_u32 s34, s40, 0x5100
	s_addc_u32 s35, s41, 0
	s_add_u32 s36, s40, 0x5200
	s_addc_u32 s37, s41, 0
	s_add_u32 s40, s40, 0x5300
	s_addc_u32 s41, s41, 0
	s_mov_b32 s48, 1
	v_mov_b32_e32 v16, 0
	s_branch .LBB0_1762

; __device__ __forceinline__ unsigned xb_add(unsigned* p, unsigned v) { return __hip_atomic_fetch_add(p, v, __ATOMIC_RELAXED, __HIP_MEMORY_SCOPE_AGENT); }
; __device__ __forceinline__ void xcd_barrier(const XcdBarrier& b) {
;     ...
;             __builtin_amdgcn_fence(__ATOMIC_ACQUIRE, "agent");
;             xb_add(&bar[XB_XGEN(b.x)], 1u);
;             asm volatile("s_waitcnt vmcnt(0)" ::: "memory");
.Lxcdlocal_3:
	s_mov_b64 s[6:7], exec
	v_mbcnt_lo_u32_b32 v0, s6, 0
	v_mbcnt_hi_u32_b32 v0, s7, v0
	v_cmp_eq_u32_e32 vcc, 0, v0
	s_waitcnt vmcnt(0)
	s_and_saveexec_b64 s[8:9], vcc
	s_cbranch_execz .LBB0_1809
	s_bcnt1_i32_b64 s6, s[6:7]
	v_mov_b32_e32 v0, 0x2000
	v_mov_b32_e32 v1, s6
	global_atomic_add v0, v1, s[4:5] offset:1024

; __device__ __forceinline__ unsigned xb_ld(unsigned* p)              { return __hip_atomic_load(p, __ATOMIC_RELAXED, __HIP_MEMORY_SCOPE_AGENT); }
; __device__ __forceinline__ bool xb_leader(int wave) { return wave == 0 && __builtin_amdgcn_mbcnt_hi(~0u, __builtin_amdgcn_mbcnt_lo(~0u, 0u)) == 0u; }
; __device__ __forceinline__ void xcd_barrier_complete(unsigned* bar, unsigned x, unsigned& nloc, unsigned& nx) {
;     const unsigned G = gridDim.x * gridDim.y * gridDim.z;
;     unsigned sum, cnt, mine, sp = 0u;
;     for (;;) {
;         sum = 0u; cnt = 0u; mine = 0u;
; #pragma unroll
;         for (unsigned j = 0; j < 16; ++j) { const unsigned c = xb_ld(&bar[XB_XCNT(j)]); sum += c; cnt += (c > 0u) ? 1u : 0u; mine = (j == x) ? c : mine; }
; __device__ __forceinline__ void xcd_barrier(const XcdBarrier& b) {
;     asm volatile("s_waitcnt vmcnt(0)" ::: "memory");
;     __syncthreads();
;     if (xb_leader(b.wave)) {
;         unsigned* bar = b.bar;
;         __builtin_amdgcn_s_waitcnt(0);
;         unsigned nloc = b.st[0], nx = b.st[1];
;         if (nloc == 0u) { xcd_barrier_complete(bar, b.x, nloc, nx); b.st[0] = nloc; b.st[1] = nx; }
.LBB0_1851:
	v_readlane_b32 s2, v254, 0
	v_readlane_b32 s3, v254, 1
	s_cmp_gt_i32 s3, 15
	s_cselect_b64 s[2:3], -1, 0
	s_and_b64 s[0:1], s[0:1], s[2:3]
	s_andn2_b64 vcc, exec, s[0:1]
	s_cbranch_vccnz .LBB0_1907
	s_waitcnt vmcnt(0)
	v_readlane_b32 s0, v254, 8
	v_readlane_b32 s1, v254, 9
	s_and_b64 vcc, exec, s[0:1]
	s_waitcnt vmcnt(0) lgkmcnt(0)
	s_barrier
	s_cbranch_vccnz .LBB0_1906
	v_mbcnt_lo_u32_b32 v0, -1, 0
	v_mbcnt_hi_u32_b32 v0, -1, v0
	v_cmp_eq_u32_e32 vcc, 0, v0
	s_and_saveexec_b64 s[0:1], vcc
	s_cbranch_execz .LBB0_1905
	s_add_i32 s4, 0, 0x23020
	v_mov_b32_e32 v0, s4
	s_waitcnt vmcnt(0) expcnt(0) lgkmcnt(0)
	buffer_inv sc1
	ds_read_b32 v2, v0
	s_add_i32 s4, 0, 0x23024
	v_mov_b32_e32 v0, s4
	ds_read_b32 v0, v0
	s_waitcnt lgkmcnt(1)
	v_cmp_ne_u32_e32 vcc, 0, v2
	s_cbranch_vccnz .LBB0_1869
	v_readlane_b32 s4, v254, 2
	v_readlane_b32 s5, v254, 3
	s_load_dwordx2 s[8:9], s[4:5], 0x4
	v_readlane_b32 s40, v254, 4
	v_readlane_b32 s41, v254, 5
	s_add_u32 s4, s40, 0x4200
	s_addc_u32 s5, s41, 0
	s_add_u32 s6, s40, 0x4400
	s_addc_u32 s7, s41, 0
	s_waitcnt lgkmcnt(0)
	s_mul_i32 s48, s8, s92
	s_add_u32 s8, s40, 0x4500
	s_mul_i32 s48, s48, s9
	s_addc_u32 s9, s41, 0
	s_add_u32 s10, s40, 0x4600
	s_addc_u32 s11, s41, 0
	s_add_u32 s12, s40, 0x4700
	s_addc_u32 s13, s41, 0
	s_add_u32 s14, s40, 0x4800
	s_addc_u32 s15, s41, 0
	s_add_u32 s16, s40, 0x4900
	s_addc_u32 s17, s41, 0
	s_add_u32 s18, s40, 0x4a00
	s_addc_u32 s19, s41, 0
	s_add_u32 s20, s40, 0x4b00
	s_addc_u32 s21, s41, 0
	s_add_u32 s22, s40, 0x4c00
	s_addc_u32 s23, s41, 0
	s_add_u32 s24, s40, 0x4d00
	s_addc_u32 s25, s41, 0
	s_add_u32 s26, s40, 0x4e00
	s_addc_u32 s27, s41, 0
	s_add_u32 s28, s40, 0x4f00
	s_addc_u32 s29, s41, 0
	s_add_u32 s30, s40, 0x5000
	s_addc_u32 s31, s41, 0
	s_add_u32 s34, s40, 0x5100
	s_addc_u32 s35, s41, 0
	s_add_u32 s36, s40, 0x5200
	s_addc_u32 s37, s41, 0
	s_add_u32 s40, s40, 0x5300
	s_addc_u32 s41, s41, 0
	s_mov_b32 s49, 1
	v_mov_b32_e32 v16, 0
	s_branch .LBB0_1857

; __device__ __forceinline__ unsigned xb_ld(unsigned* p)              { return __hip_atomic_load(p, __ATOMIC_RELAXED, __HIP_MEMORY_SCOPE_AGENT); }
; __device__ __forceinline__ bool xb_leader(int wave) { return wave == 0 && __builtin_amdgcn_mbcnt_hi(~0u, __builtin_amdgcn_mbcnt_lo(~0u, 0u)) == 0u; }
; __device__ __forceinline__ void xcd_barrier_complete(unsigned* bar, unsigned x, unsigned& nloc, unsigned& nx) {
;     const unsigned G = gridDim.x * gridDim.y * gridDim.z;
;     unsigned sum, cnt, mine, sp = 0u;
;     for (;;) {
;         sum = 0u; cnt = 0u; mine = 0u;
; #pragma unroll
;         for (unsigned j = 0; j < 16; ++j) { const unsigned c = xb_ld(&bar[XB_XCNT(j)]); sum += c; cnt += (c > 0u) ? 1u : 0u; mine = (j == x) ? c : mine; }
; __device__ __forceinline__ void xcd_barrier(const XcdBarrier& b) {
;     asm volatile("s_waitcnt vmcnt(0)" ::: "memory");
;     __syncthreads();
;     if (xb_leader(b.wave)) {
;         unsigned* bar = b.bar;
;         __builtin_amdgcn_s_waitcnt(0);
;         unsigned nloc = b.st[0], nx = b.st[1];
;         if (nloc == 0u) { xcd_barrier_complete(bar, b.x, nloc, nx); b.st[0] = nloc; b.st[1] = nx; }
.LBB0_2022:
	v_readlane_b32 s2, v254, 0
	v_readlane_b32 s3, v254, 1
	s_cmp_gt_i32 s3, 16
	s_cselect_b64 s[2:3], -1, 0
	s_and_b64 s[0:1], s[0:1], s[2:3]
	s_andn2_b64 vcc, exec, s[0:1]
	s_cbranch_vccnz .LBB0_2078
	s_waitcnt vmcnt(0)
	v_readlane_b32 s0, v254, 8
	v_readlane_b32 s1, v254, 9
	s_and_b64 vcc, exec, s[0:1]
	s_waitcnt vmcnt(0) lgkmcnt(0)
	s_barrier
	s_cbranch_vccnz .LBB0_2077
	v_mbcnt_lo_u32_b32 v0, -1, 0
	v_mbcnt_hi_u32_b32 v0, -1, v0
	v_cmp_eq_u32_e32 vcc, 0, v0
	s_and_saveexec_b64 s[0:1], vcc
	s_cbranch_execz .LBB0_2076
	s_add_i32 s4, 0, 0x23020
	v_mov_b32_e32 v0, s4
	s_waitcnt vmcnt(0) expcnt(0) lgkmcnt(0)
	buffer_inv sc1
	ds_read_b32 v2, v0
	s_add_i32 s4, 0, 0x23024
	v_mov_b32_e32 v0, s4
	ds_read_b32 v0, v0
	s_waitcnt lgkmcnt(1)
	v_cmp_ne_u32_e32 vcc, 0, v2
	s_cbranch_vccnz .LBB0_2040
	v_readlane_b32 s4, v254, 2
	v_readlane_b32 s5, v254, 3
	s_load_dwordx2 s[8:9], s[4:5], 0x4
	v_readlane_b32 s40, v254, 4
	v_readlane_b32 s41, v254, 5
	s_add_u32 s4, s40, 0x4200
	s_addc_u32 s5, s41, 0
	s_add_u32 s6, s40, 0x4400
	s_addc_u32 s7, s41, 0
	s_waitcnt lgkmcnt(0)
	s_mul_i32 s33, s8, s92
	s_add_u32 s8, s40, 0x4500
	s_mul_i32 s33, s33, s9
	s_addc_u32 s9, s41, 0
	s_add_u32 s10, s40, 0x4600
	s_addc_u32 s11, s41, 0
	s_add_u32 s12, s40, 0x4700
	s_addc_u32 s13, s41, 0
	s_add_u32 s14, s40, 0x4800
	s_addc_u32 s15, s41, 0
	s_add_u32 s16, s40, 0x4900
	s_addc_u32 s17, s41, 0
	s_add_u32 s18, s40, 0x4a00
	s_addc_u32 s19, s41, 0
	s_add_u32 s20, s40, 0x4b00
	s_addc_u32 s21, s41, 0
	s_add_u32 s22, s40, 0x4c00
	s_addc_u32 s23, s41, 0
	s_add_u32 s24, s40, 0x4d00
	s_addc_u32 s25, s41, 0
	s_add_u32 s26, s40, 0x4e00
	s_addc_u32 s27, s41, 0
	s_add_u32 s28, s40, 0x4f00
	s_addc_u32 s29, s41, 0
	s_add_u32 s30, s40, 0x5000
	s_addc_u32 s31, s41, 0
	s_add_u32 s34, s40, 0x5100
	s_addc_u32 s35, s41, 0
	s_add_u32 s36, s40, 0x5200
	s_addc_u32 s37, s41, 0
	s_add_u32 s40, s40, 0x5300
	s_addc_u32 s41, s41, 0
	s_mov_b32 s48, 1
	v_mov_b32_e32 v16, 0
	s_branch .LBB0_2028

; __device__ __forceinline__ unsigned xb_ld(unsigned* p)              { return __hip_atomic_load(p, __ATOMIC_RELAXED, __HIP_MEMORY_SCOPE_AGENT); }
; __device__ __forceinline__ bool xb_leader(int wave) { return wave == 0 && __builtin_amdgcn_mbcnt_hi(~0u, __builtin_amdgcn_mbcnt_lo(~0u, 0u)) == 0u; }
; __device__ __forceinline__ void xcd_barrier_complete(unsigned* bar, unsigned x, unsigned& nloc, unsigned& nx) {
;     const unsigned G = gridDim.x * gridDim.y * gridDim.z;
;     unsigned sum, cnt, mine, sp = 0u;
;     for (;;) {
;         sum = 0u; cnt = 0u; mine = 0u;
; #pragma unroll
;         for (unsigned j = 0; j < 16; ++j) { const unsigned c = xb_ld(&bar[XB_XCNT(j)]); sum += c; cnt += (c > 0u) ? 1u : 0u; mine = (j == x) ? c : mine; }
; __device__ __forceinline__ void xcd_barrier(const XcdBarrier& b) {
;     asm volatile("s_waitcnt vmcnt(0)" ::: "memory");
;     __syncthreads();
;     if (xb_leader(b.wave)) {
;         unsigned* bar = b.bar;
;         __builtin_amdgcn_s_waitcnt(0);
;         unsigned nloc = b.st[0], nx = b.st[1];
;         if (nloc == 0u) { xcd_barrier_complete(bar, b.x, nloc, nx); b.st[0] = nloc; b.st[1] = nx; }
.LBB0_2102:
	v_readlane_b32 s2, v254, 0
	v_readlane_b32 s3, v254, 1
	s_cmp_gt_i32 s3, 17
	s_cselect_b64 s[2:3], -1, 0
	s_and_b64 s[0:1], s[0:1], s[2:3]
	s_andn2_b64 vcc, exec, s[0:1]
	s_cbranch_vccnz .LBB0_2158
	s_waitcnt vmcnt(0)
	v_readlane_b32 s0, v254, 8
	v_readlane_b32 s1, v254, 9
	s_and_b64 vcc, exec, s[0:1]
	s_waitcnt vmcnt(0) lgkmcnt(0)
	s_barrier
	s_cbranch_vccnz .LBB0_2157
	v_mbcnt_lo_u32_b32 v0, -1, 0
	v_mbcnt_hi_u32_b32 v0, -1, v0
	v_cmp_eq_u32_e32 vcc, 0, v0
	s_and_saveexec_b64 s[0:1], vcc
	s_cbranch_execz .LBB0_2156
	s_add_i32 s4, 0, 0x23020
	v_mov_b32_e32 v0, s4
	s_waitcnt vmcnt(0) expcnt(0) lgkmcnt(0)
	buffer_inv sc1
	ds_read_b32 v2, v0
	s_add_i32 s4, 0, 0x23024
	v_mov_b32_e32 v0, s4
	ds_read_b32 v0, v0
	s_waitcnt lgkmcnt(1)
	v_cmp_ne_u32_e32 vcc, 0, v2
	s_cbranch_vccnz .LBB0_2120
	v_readlane_b32 s4, v254, 2
	v_readlane_b32 s5, v254, 3
	s_load_dwordx2 s[8:9], s[4:5], 0x4
	v_readlane_b32 s40, v254, 4
	v_readlane_b32 s41, v254, 5
	s_add_u32 s4, s40, 0x4200
	s_addc_u32 s5, s41, 0
	s_add_u32 s6, s40, 0x4400
	s_addc_u32 s7, s41, 0
	s_waitcnt lgkmcnt(0)
	s_mul_i32 s49, s8, s92
	s_add_u32 s8, s40, 0x4500
	s_mul_i32 s49, s49, s9
	s_addc_u32 s9, s41, 0
	s_add_u32 s10, s40, 0x4600
	s_addc_u32 s11, s41, 0
	s_add_u32 s12, s40, 0x4700
	s_addc_u32 s13, s41, 0
	s_add_u32 s14, s40, 0x4800
	s_addc_u32 s15, s41, 0
	s_add_u32 s16, s40, 0x4900
	s_addc_u32 s17, s41, 0
	s_add_u32 s18, s40, 0x4a00
	s_addc_u32 s19, s41, 0
	s_add_u32 s20, s40, 0x4b00
	s_addc_u32 s21, s41, 0
	s_add_u32 s22, s40, 0x4c00
	s_addc_u32 s23, s41, 0
	s_add_u32 s24, s40, 0x4d00
	s_addc_u32 s25, s41, 0
	s_add_u32 s26, s40, 0x4e00
	s_addc_u32 s27, s41, 0
	s_add_u32 s28, s40, 0x4f00
	s_addc_u32 s29, s41, 0
	s_add_u32 s30, s40, 0x5000
	s_addc_u32 s31, s41, 0
	s_add_u32 s34, s40, 0x5100
	s_addc_u32 s35, s41, 0
	s_add_u32 s36, s40, 0x5200
	s_addc_u32 s37, s41, 0
	s_add_u32 s40, s40, 0x5300
	s_addc_u32 s41, s41, 0
	s_mov_b32 s50, 1
	v_mov_b32_e32 v16, 0
	s_branch .LBB0_2108

; __device__ __forceinline__ unsigned xb_ld(unsigned* p)              { return __hip_atomic_load(p, __ATOMIC_RELAXED, __HIP_MEMORY_SCOPE_AGENT); }
; __device__ __forceinline__ bool xb_leader(int wave) { return wave == 0 && __builtin_amdgcn_mbcnt_hi(~0u, __builtin_amdgcn_mbcnt_lo(~0u, 0u)) == 0u; }
; __device__ __forceinline__ void xcd_barrier_complete(unsigned* bar, unsigned x, unsigned& nloc, unsigned& nx) {
;     const unsigned G = gridDim.x * gridDim.y * gridDim.z;
;     unsigned sum, cnt, mine, sp = 0u;
;     for (;;) {
;         sum = 0u; cnt = 0u; mine = 0u;
; #pragma unroll
;         for (unsigned j = 0; j < 16; ++j) { const unsigned c = xb_ld(&bar[XB_XCNT(j)]); sum += c; cnt += (c > 0u) ? 1u : 0u; mine = (j == x) ? c : mine; }
; __device__ __forceinline__ void xcd_barrier(const XcdBarrier& b) {
;     asm volatile("s_waitcnt vmcnt(0)" ::: "memory");
;     __syncthreads();
;     if (xb_leader(b.wave)) {
;         unsigned* bar = b.bar;
;         __builtin_amdgcn_s_waitcnt(0);
;         unsigned nloc = b.st[0], nx = b.st[1];
;         if (nloc == 0u) { xcd_barrier_complete(bar, b.x, nloc, nx); b.st[0] = nloc; b.st[1] = nx; }
.LBB0_2211:
	v_readlane_b32 s2, v254, 0
	v_readlane_b32 s3, v254, 1
	s_cmp_gt_i32 s3, 18
	s_cselect_b64 s[2:3], -1, 0
	s_and_b64 s[0:1], s[0:1], s[2:3]
	s_andn2_b64 vcc, exec, s[0:1]
	s_cbranch_vccnz .LBB0_2267
	s_waitcnt vmcnt(0)
	v_readlane_b32 s0, v254, 8
	v_readlane_b32 s1, v254, 9
	s_and_b64 vcc, exec, s[0:1]
	s_waitcnt vmcnt(0) lgkmcnt(0)
	s_barrier
	s_cbranch_vccnz .LBB0_2266
	v_mbcnt_lo_u32_b32 v0, -1, 0
	v_mbcnt_hi_u32_b32 v0, -1, v0
	v_cmp_eq_u32_e32 vcc, 0, v0
	s_and_saveexec_b64 s[0:1], vcc
	s_cbranch_execz .LBB0_2265
	s_add_i32 s4, 0, 0x23020
	v_mov_b32_e32 v0, s4
	s_waitcnt vmcnt(0) expcnt(0) lgkmcnt(0)
	buffer_inv sc1
	ds_read_b32 v2, v0
	s_add_i32 s4, 0, 0x23024
	v_mov_b32_e32 v0, s4
	ds_read_b32 v0, v0
	s_waitcnt lgkmcnt(1)
	v_cmp_ne_u32_e32 vcc, 0, v2
	s_cbranch_vccnz .LBB0_2229
	v_readlane_b32 s4, v254, 2
	v_readlane_b32 s5, v254, 3
	s_load_dwordx2 s[8:9], s[4:5], 0x4
	v_readlane_b32 s38, v254, 4
	v_readlane_b32 s39, v254, 5
	s_add_u32 s4, s38, 0x4200
	s_addc_u32 s5, s39, 0
	s_add_u32 s6, s38, 0x4400
	s_addc_u32 s7, s39, 0
	s_waitcnt lgkmcnt(0)
	s_mul_i32 s33, s8, s92
	s_add_u32 s8, s38, 0x4500
	s_mul_i32 s33, s33, s9
	s_addc_u32 s9, s39, 0
	s_add_u32 s10, s38, 0x4600
	s_addc_u32 s11, s39, 0
	s_add_u32 s12, s38, 0x4700
	s_addc_u32 s13, s39, 0
	s_add_u32 s14, s38, 0x4800
	s_addc_u32 s15, s39, 0
	s_add_u32 s16, s38, 0x4900
	s_addc_u32 s17, s39, 0
	s_add_u32 s18, s38, 0x4a00
	s_addc_u32 s19, s39, 0
	s_add_u32 s20, s38, 0x4b00
	s_addc_u32 s21, s39, 0
	s_add_u32 s22, s38, 0x4c00
	s_addc_u32 s23, s39, 0
	s_add_u32 s24, s38, 0x4d00
	s_addc_u32 s25, s39, 0
	s_add_u32 s26, s38, 0x4e00
	s_addc_u32 s27, s39, 0
	s_add_u32 s28, s38, 0x4f00
	s_addc_u32 s29, s39, 0
	s_add_u32 s30, s38, 0x5000
	s_addc_u32 s31, s39, 0
	s_add_u32 s34, s38, 0x5100
	s_addc_u32 s35, s39, 0
	s_add_u32 s36, s38, 0x5200
	s_addc_u32 s37, s39, 0
	s_add_u32 s38, s38, 0x5300
	s_addc_u32 s39, s39, 0
	s_mov_b32 s46, 1
	v_mov_b32_e32 v16, 0
	s_branch .LBB0_2217
